# v37 + MLA P.V stage: first four V-fragment LDS reads issued behind the third QK MFMA (v224-239), blanket lgkmcnt(0) of the macro dropped, hipcc counted waits kept
# speedup vs baseline: 1.0147x; 1.0147x over previous
.LBB0_565:
	s_waitcnt lgkmcnt(4)
	v_mfma_scale_f32_32x32x64_f8f6f4 v[96:111], v[96:103], v[120:127], 0, v205, v205 op_sel_hi:[0,0,0]
	v_cndmask_b32_e64 v176, v189, v192, s[4:5]
	v_fma_f32 v80, v80, s40, -v176
	v_fma_f32 v81, v81, s40, -v176
	v_fma_f32 v84, v84, s40, -v176
	v_fma_f32 v85, v85, s40, -v176
	v_fma_f32 v88, v88, s40, -v176
	v_fma_f32 v89, v89, s40, -v176
	v_fma_f32 v92, v92, s40, -v176
	v_fma_f32 v93, v93, s40, -v176
	v_exp_f32_e32 v80, v80
	v_exp_f32_e32 v81, v81
	v_exp_f32_e32 v84, v84
	v_exp_f32_e32 v85, v85
	v_exp_f32_e32 v88, v88
	v_exp_f32_e32 v89, v89
	s_waitcnt lgkmcnt(2)
	v_mfma_scale_f32_32x32x64_f8f6f4 v[96:111], v[156:163], v[128:135], v[96:111], v205, v205 op_sel_hi:[0,0,0]
	v_exp_f32_e32 v92, v92
	v_exp_f32_e32 v93, v93
	v_fma_f32 v82, v82, s40, -v176
	v_fma_f32 v83, v83, s40, -v176
	v_fma_f32 v86, v86, s40, -v176
	v_fma_f32 v87, v87, s40, -v176
	v_fma_f32 v90, v90, s40, -v176
	v_fma_f32 v91, v91, s40, -v176
	v_fma_f32 v94, v94, s40, -v176
	v_fma_f32 v95, v95, s40, -v176
	v_exp_f32_e32 v82, v82
	v_exp_f32_e32 v83, v83
	v_exp_f32_e32 v86, v86
	v_exp_f32_e32 v87, v87
	v_exp_f32_e32 v90, v90
	s_waitcnt lgkmcnt(0)
	v_mfma_scale_f32_32x32x64_f8f6f4 v[96:111], v[148:155], v[136:143], v[96:111], v205, v205 op_sel_hi:[0,0,0]
	v_lshl_add_u32 v240, s23, 14, v211
	ds_read_b128 v[224:227], v240
	ds_read_b128 v[228:231], v240 offset:16
	ds_read_b128 v[232:235], v240 offset:2560
	ds_read_b128 v[236:239], v240 offset:2576
	v_mov_b32_e32 v148, 0
	v_mov_b32_e32 v149, 0
	v_mov_b32_e32 v150, 0
	v_mov_b32_e32 v151, 0
	v_exp_f32_e32 v91, v91
	v_exp_f32_e32 v94, v94
	v_exp_f32_e32 v95, v95
	v_cvt_pk_fp8_f32 v148, v80, v81
	v_cvt_pk_fp8_f32 v149, v84, v85
	v_cvt_pk_fp8_f32 v150, v88, v89
	v_cvt_pk_fp8_f32 v151, v92, v93
	v_lshl_add_u32 v156, s23, 14, v211
	v_cvt_pk_fp8_f32 v148, v82, v83 op_sel:[0,0,1]
	v_cvt_pk_fp8_f32 v149, v86, v87 op_sel:[0,0,1]
	v_cvt_pk_fp8_f32 v150, v90, v91 op_sel:[0,0,1]
	v_cvt_pk_fp8_f32 v151, v94, v95 op_sel:[0,0,1]
	s_waitcnt lgkmcnt(2)
	v_mfma_scale_f32_32x32x64_f8f6f4 v[48:63], v[144:151], v[224:231], v[48:63], v205, v205 op_sel_hi:[0,0,0]
	ds_read_b128 v[80:83], v156 offset:5120
	ds_read_b128 v[84:87], v156 offset:5136
	ds_read_b128 v[152:155], v156 offset:7680
	ds_read_b128 v[156:159], v156 offset:7696
	s_waitcnt lgkmcnt(4)
	v_mfma_scale_f32_32x32x64_f8f6f4 v[32:47], v[144:151], v[232:239], v[32:47], v205, v205 op_sel_hi:[0,0,0]
	v_max_f32_e32 v88, v97, v97
	v_max_f32_e32 v89, v96, v96
	v_max_f32_e32 v88, v89, v88
	v_max3_f32 v88, v88, v98, v99
	v_max3_f32 v88, v88, v100, v101
	v_max3_f32 v88, v88, v102, v103
	v_max3_f32 v88, v88, v104, v105
	v_max3_f32 v88, v88, v106, v107
	s_waitcnt lgkmcnt(2)
	v_mfma_scale_f32_32x32x64_f8f6f4 v[16:31], v[144:151], v[80:87], v[16:31], v205, v205 op_sel_hi:[0,0,0]
	v_max3_f32 v88, v88, v108, v109
	v_max3_f32 v88, v88, v110, v111
	v_mov_b32_e32 v89, v88
	s_nop 1
	v_permlane32_swap_b32_e32 v88, v89
	v_max_f32_e32 v80, v89, v89
	v_max_f32_e32 v81, v88, v88
	v_max_f32_e32 v80, v81, v80
	v_fma_f32 v81, v80, s40, -v176
	v_cmp_ge_f32_e32 vcc, s70, v81
	v_fmamk_f32 v80, v80, 0x3dd53b94, v202
	v_max_f32_e32 v81, v176, v176
	v_max_f32_e32 v80, v81, v80
	v_sub_f32_e32 v81, v176, v80
	v_exp_f32_e32 v81, v81
	s_waitcnt lgkmcnt(0)
	v_mfma_scale_f32_32x32x64_f8f6f4 v[0:15], v[144:151], v[152:159], v[0:15], v205, v205 op_sel_hi:[0,0,0]
	s_cmp_eq_u64 vcc, exec
	s_cselect_b64 vcc, -1, 0
	v_cndmask_b32_e32 v192, v80, v176, vcc
	s_add_i32 s21, s21, 2
	s_add_i32 s78, s78, 1
	s_add_i32 s22, s22, 64
	v_fma_f32 v178, v96, s40, -v192
	v_fma_f32 v179, v97, s40, -v192
	v_fma_f32 v176, v98, s40, -v192
	v_fma_f32 v177, v99, s40, -v192
	v_fma_f32 v162, v100, s40, -v192
	v_fma_f32 v163, v101, s40, -v192
	v_fma_f32 v160, v102, s40, -v192
	v_fma_f32 v161, v103, s40, -v192
	v_pk_fma_f32 v[158:159], v[104:105], s[40:41], v[192:193] op_sel_hi:[1,0,0] neg_lo:[0,0,1] neg_hi:[0,0,1]
	v_pk_fma_f32 v[156:157], v[106:107], s[40:41], v[192:193] op_sel_hi:[1,0,0] neg_lo:[0,0,1] neg_hi:[0,0,1]
	v_pk_fma_f32 v[154:155], v[108:109], s[40:41], v[192:193] op_sel_hi:[1,0,0] neg_lo:[0,0,1] neg_hi:[0,0,1]
	v_pk_fma_f32 v[152:153], v[110:111], s[40:41], v[192:193] op_sel_hi:[1,0,0] neg_lo:[0,0,1] neg_hi:[0,0,1]
	v_cndmask_b32_e64 v88, v81, 1.0, vcc
	v_mfma_scale_f32_32x32x64_f8f6f4 v[64:79], v[144:151], v[112:119], v[64:79], v205, v205 op_sel_hi:[0,0,0]
	s_cmp_ge_u32 s21, s17
	s_barrier
	s_cbranch_scc1 .LBB0_580

.LBB0_1875:
	s_waitcnt lgkmcnt(4)
	v_mfma_scale_f32_32x32x64_f8f6f4 v[96:111], v[96:103], v[120:127], 0, v207, v207 op_sel_hi:[0,0,0]
	v_cndmask_b32_e64 v176, v191, v194, s[4:5]
	v_fma_f32 v80, v80, s38, -v176
	v_fma_f32 v81, v81, s38, -v176
	v_fma_f32 v84, v84, s38, -v176
	v_fma_f32 v85, v85, s38, -v176
	v_fma_f32 v88, v88, s38, -v176
	v_fma_f32 v89, v89, s38, -v176
	v_fma_f32 v92, v92, s38, -v176
	v_fma_f32 v93, v93, s38, -v176
	v_exp_f32_e32 v80, v80
	v_exp_f32_e32 v81, v81
	v_exp_f32_e32 v84, v84
	v_exp_f32_e32 v85, v85
	v_exp_f32_e32 v88, v88
	v_exp_f32_e32 v89, v89
	s_waitcnt lgkmcnt(2)
	v_mfma_scale_f32_32x32x64_f8f6f4 v[96:111], v[156:163], v[128:135], v[96:111], v207, v207 op_sel_hi:[0,0,0]
	v_exp_f32_e32 v92, v92
	v_exp_f32_e32 v93, v93
	v_fma_f32 v82, v82, s38, -v176
	v_fma_f32 v83, v83, s38, -v176
	v_fma_f32 v86, v86, s38, -v176
	v_fma_f32 v87, v87, s38, -v176
	v_fma_f32 v90, v90, s38, -v176
	v_fma_f32 v91, v91, s38, -v176
	v_fma_f32 v94, v94, s38, -v176
	v_fma_f32 v95, v95, s38, -v176
	v_exp_f32_e32 v82, v82
	v_exp_f32_e32 v83, v83
	v_exp_f32_e32 v86, v86
	v_exp_f32_e32 v87, v87
	v_exp_f32_e32 v90, v90
	s_waitcnt lgkmcnt(0)
	v_mfma_scale_f32_32x32x64_f8f6f4 v[96:111], v[148:155], v[136:143], v[96:111], v207, v207 op_sel_hi:[0,0,0]
	v_lshl_add_u32 v240, s24, 14, v209
	ds_read_b128 v[224:227], v240
	ds_read_b128 v[228:231], v240 offset:16
	ds_read_b128 v[232:235], v240 offset:2560
	ds_read_b128 v[236:239], v240 offset:2576
	v_mov_b32_e32 v148, 0
	v_mov_b32_e32 v149, 0
	v_mov_b32_e32 v150, 0
	v_mov_b32_e32 v151, 0
	v_exp_f32_e32 v91, v91
	v_exp_f32_e32 v94, v94
	v_exp_f32_e32 v95, v95
	v_cvt_pk_fp8_f32 v148, v80, v81
	v_cvt_pk_fp8_f32 v149, v84, v85
	v_cvt_pk_fp8_f32 v150, v88, v89
	v_cvt_pk_fp8_f32 v151, v92, v93
	v_lshl_add_u32 v156, s24, 14, v209
	v_cvt_pk_fp8_f32 v148, v82, v83 op_sel:[0,0,1]
	v_cvt_pk_fp8_f32 v149, v86, v87 op_sel:[0,0,1]
	v_cvt_pk_fp8_f32 v150, v90, v91 op_sel:[0,0,1]
	v_cvt_pk_fp8_f32 v151, v94, v95 op_sel:[0,0,1]
	s_waitcnt lgkmcnt(2)
	v_mfma_scale_f32_32x32x64_f8f6f4 v[48:63], v[144:151], v[224:231], v[48:63], v207, v207 op_sel_hi:[0,0,0]
	ds_read_b128 v[80:83], v156 offset:5120
	ds_read_b128 v[84:87], v156 offset:5136
	ds_read_b128 v[152:155], v156 offset:7680
	ds_read_b128 v[156:159], v156 offset:7696
	s_waitcnt lgkmcnt(4)
	v_mfma_scale_f32_32x32x64_f8f6f4 v[32:47], v[144:151], v[232:239], v[32:47], v207, v207 op_sel_hi:[0,0,0]
	v_max_f32_e32 v88, v97, v97
	v_max_f32_e32 v89, v96, v96
	v_max_f32_e32 v88, v89, v88
	v_max3_f32 v88, v88, v98, v99
	v_max3_f32 v88, v88, v100, v101
	v_max3_f32 v88, v88, v102, v103
	v_max3_f32 v88, v88, v104, v105
	v_max3_f32 v88, v88, v106, v107
	s_waitcnt lgkmcnt(2)
	v_mfma_scale_f32_32x32x64_f8f6f4 v[16:31], v[144:151], v[80:87], v[16:31], v207, v207 op_sel_hi:[0,0,0]
	v_max3_f32 v88, v88, v108, v109
	v_max3_f32 v88, v88, v110, v111
	v_mov_b32_e32 v89, v88
	s_nop 1
	v_permlane32_swap_b32_e32 v88, v89
	v_max_f32_e32 v80, v89, v89
	v_max_f32_e32 v81, v88, v88
	v_max_f32_e32 v80, v81, v80
	v_fma_f32 v81, v80, s38, -v176
	v_cmp_ge_f32_e32 vcc, s68, v81
	v_fmamk_f32 v80, v80, 0x3dd53b94, v204
	v_max_f32_e32 v81, v176, v176
	v_max_f32_e32 v80, v81, v80
	v_sub_f32_e32 v81, v176, v80
	v_exp_f32_e32 v81, v81
	s_waitcnt lgkmcnt(0)
	v_mfma_scale_f32_32x32x64_f8f6f4 v[0:15], v[144:151], v[152:159], v[0:15], v207, v207 op_sel_hi:[0,0,0]
	s_cmp_eq_u64 vcc, exec
	s_cselect_b64 vcc, -1, 0
	v_cndmask_b32_e32 v194, v80, v176, vcc
	v_fma_f32 v178, v96, s38, -v194
	v_fma_f32 v179, v97, s38, -v194
	v_fma_f32 v176, v98, s38, -v194
	v_fma_f32 v177, v99, s38, -v194
	v_fma_f32 v162, v100, s38, -v194
	v_fma_f32 v163, v101, s38, -v194
	v_fma_f32 v160, v102, s38, -v194
	v_fma_f32 v161, v103, s38, -v194
	v_fma_f32 v158, v104, s38, -v194
	v_fma_f32 v159, v105, s38, -v194
	v_pk_fma_f32 v[156:157], v[106:107], s[38:39], v[194:195] op_sel_hi:[1,0,0] neg_lo:[0,0,1] neg_hi:[0,0,1]
	v_pk_fma_f32 v[154:155], v[108:109], s[38:39], v[194:195] op_sel_hi:[1,0,0] neg_lo:[0,0,1] neg_hi:[0,0,1]
	v_pk_fma_f32 v[152:153], v[110:111], s[38:39], v[194:195] op_sel_hi:[1,0,0] neg_lo:[0,0,1] neg_hi:[0,0,1]
	v_cndmask_b32_e64 v88, v81, 1.0, vcc
	s_add_i32 s17, s17, 2
	s_add_i32 s76, s76, 1
	s_and_b64 vcc, exec, s[18:19]
	v_mfma_scale_f32_32x32x64_f8f6f4 v[64:79], v[144:151], v[112:119], v[64:79], v207, v207 op_sel_hi:[0,0,0]
	s_barrier
	s_cbranch_vccnz .LBB0_1889
